# P0 activation quantisation row loop software-pipelined: next row's loads prefetched into v60..v91 one iteration ahead
# baseline (speedup 1.0000x reference)
.LBB0_65:
	s_lshl_b32 s0, s96, 3
	s_add_i32 s0, s0, s86
	v_readlane_b32 s52, v254, 32
	s_cmpk_gt_i32 s0, 0x3fff
	v_readlane_b32 s53, v254, 33
	v_readlane_b32 s54, v254, 34
	v_readlane_b32 s55, v254, 35
	v_readlane_b32 s56, v254, 36
	v_readlane_b32 s57, v254, 37
	v_readlane_b32 s58, v254, 38
	v_readlane_b32 s59, v254, 39
	v_readlane_b32 s60, v254, 40
	v_readlane_b32 s61, v254, 41
	v_readlane_b32 s62, v254, 42
	v_readlane_b32 s63, v254, 43
	v_readlane_b32 s64, v254, 44
	v_readlane_b32 s65, v254, 45
	v_readlane_b32 s66, v254, 46
	v_readlane_b32 s67, v254, 47
	s_cbranch_scc1 .LBB0_70
	s_ashr_i32 s1, s0, 31
	s_lshl_b32 s4, s90, 3
	s_lshl_b64 s[8:9], s[0:1], 2
	s_add_u32 s3, s8, 0x181000
	s_addc_u32 s16, s9, 0
	s_ashr_i32 s5, s4, 31
	s_lshl_b64 s[10:11], s[0:1], 11
	s_lshl_b64 s[8:9], s[4:5], 2
	v_lshl_or_b32 v14, v1, 2, s10
	v_mov_b32_e32 v15, s11
	s_lshl_b64 s[10:11], s[4:5], 11
	s_lshl_b64 s[12:13], s[0:1], 13
	v_readlane_b32 s36, v254, 13
	v_readlane_b32 s37, v254, 14
	s_add_u32 s12, s36, s12
	v_lshlrev_b32_e32 v16, 4, v1
	v_mov_b32_e32 v17, 0
	s_addc_u32 s13, s37, s13
	v_lshl_add_u64 v[2:3], s[12:13], 0, v[16:17]
	s_mov_b64 s[12:13], 0x1000
	v_cmp_eq_u32_e64 s[6:7], 0, v1
	v_lshl_add_u64 v[18:19], v[2:3], 0, s[12:13]
	s_lshl_b64 s[12:13], s[4:5], 13
	s_mov_b32 s1, 0x42fe0000
	s_mov_b32 s5, 0x40c0c00
	s_mov_b32 s17, 0x5400000
	v_readlane_b32 s38, v254, 15
	v_readlane_b32 s39, v254, 16
	v_readlane_b32 s40, v254, 17
	v_readlane_b32 s41, v254, 18
	v_readlane_b32 s42, v254, 19
	v_readlane_b32 s43, v254, 20
	v_readlane_b32 s44, v254, 21
	v_readlane_b32 s45, v254, 22
	v_readlane_b32 s46, v254, 23
	v_readlane_b32 s47, v254, 24
	v_readlane_b32 s48, v254, 25
	v_readlane_b32 s49, v254, 26
	v_readlane_b32 s50, v254, 27
	v_readlane_b32 s51, v254, 28
	global_load_dwordx4 v[60:63], v[18:19], off offset:-4096
	global_load_dwordx4 v[64:67], v[18:19], off offset:-3072
	global_load_dwordx4 v[68:71], v[18:19], off offset:-2048
	global_load_dwordx4 v[72:75], v[18:19], off offset:-1024
	global_load_dwordx4 v[76:79], v[18:19], off
	global_load_dwordx4 v[80:83], v[18:19], off offset:1024
	global_load_dwordx4 v[84:87], v[18:19], off offset:2048
	global_load_dwordx4 v[88:91], v[18:19], off offset:3072
	s_waitcnt vmcnt(0)
	s_branch .LBB0_68

.LBB0_68:
	s_add_i32 s99, s0, s4
	s_cmpk_lt_i32 s99, 0x4000
	s_cselect_b32 s100, s12, 0
	s_cselect_b32 s101, s13, 0
	v_lshl_add_u64 v[92:93], v[18:19], 0, s[100:101]
	s_waitcnt vmcnt(8)
	v_mov_b64_e32 v[20:21], v[60:61]
	v_mov_b64_e32 v[22:23], v[62:63]
	v_mov_b64_e32 v[24:25], v[64:65]
	v_mov_b64_e32 v[26:27], v[66:67]
	v_mov_b64_e32 v[28:29], v[68:69]
	v_mov_b64_e32 v[30:31], v[70:71]
	v_mov_b64_e32 v[32:33], v[72:73]
	v_mov_b64_e32 v[34:35], v[74:75]
	v_mov_b64_e32 v[36:37], v[76:77]
	v_mov_b64_e32 v[38:39], v[78:79]
	v_mov_b64_e32 v[10:11], v[80:81]
	v_mov_b64_e32 v[12:13], v[82:83]
	v_mov_b64_e32 v[6:7], v[84:85]
	v_mov_b64_e32 v[8:9], v[86:87]
	v_mov_b64_e32 v[2:3], v[88:89]
	v_mov_b64_e32 v[4:5], v[90:91]
	global_load_dwordx4 v[60:63], v[92:93], off offset:-4096
	global_load_dwordx4 v[64:67], v[92:93], off offset:-3072
	global_load_dwordx4 v[68:71], v[92:93], off offset:-2048
	global_load_dwordx4 v[72:75], v[92:93], off offset:-1024
	global_load_dwordx4 v[76:79], v[92:93], off
	global_load_dwordx4 v[80:83], v[92:93], off offset:1024
	global_load_dwordx4 v[84:87], v[92:93], off offset:2048
	global_load_dwordx4 v[88:91], v[92:93], off offset:3072
	v_lshl_add_u64 v[40:41], s[92:93], 0, v[14:15]
	v_add_co_u32_e32 v40, vcc, s17, v40
	v_max_f32_e64 v16, |v23|, |v23|
	v_max_f32_e64 v42, |v22|, |v22|
	v_max_f32_e64 v43, |v27|, |v27|
	v_max_f32_e64 v44, |v26|, |v26|
	v_max_f32_e64 v45, |v31|, |v31|
	v_max_f32_e64 v46, |v30|, |v30|
	v_max_f32_e64 v47, |v35|, |v35|
	v_max_f32_e64 v48, |v34|, |v34|
	v_max_f32_e32 v16, v42, v16
	v_max_f32_e32 v42, v44, v43
	v_max_f32_e64 v49, |v39|, |v39|
	v_max_f32_e64 v50, |v38|, |v38|
	v_max_f32_e64 v51, |v13|, |v13|
	v_max_f32_e64 v52, |v12|, |v12|
	v_max_f32_e32 v43, v46, v45
	v_max_f32_e32 v44, v48, v47
	v_max3_f32 v16, |v20|, |v21|, v16
	v_max3_f32 v42, |v24|, |v25|, v42
	v_max_f32_e64 v53, |v9|, |v9|
	v_max_f32_e64 v54, |v8|, |v8|
	v_max_f32_e64 v55, |v5|, |v5|
	v_max_f32_e64 v56, |v4|, |v4|
	v_max_f32_e32 v45, v50, v49
	v_max_f32_e32 v46, v52, v51
	v_max3_f32 v43, |v28|, |v29|, v43
	v_max3_f32 v44, |v32|, |v33|, v44
	v_max3_f32 v16, v16, 0, v42
	v_max_f32_e32 v47, v54, v53
	v_max_f32_e32 v48, v56, v55
	v_max3_f32 v45, |v36|, |v37|, v45
	v_max3_f32 v46, |v10|, |v11|, v46
	v_max3_f32 v16, v16, v43, v44
	v_max3_f32 v47, |v6|, |v7|, v47
	v_max3_f32 v48, |v2|, |v3|, v48
	v_max3_f32 v16, v16, v45, v46
	v_max3_f32 v16, v16, v47, v48
	v_addc_co_u32_e32 v41, vcc, 0, v41, vcc
	s_nop 0
	v_mov_b32_dpp v42, v16 quad_perm:[1,0,3,2] row_mask:0xf bank_mask:0xf bound_ctrl:1
	v_max_f32_e32 v42, v42, v42
	v_max_f32_e32 v16, v16, v42
	s_nop 1
	v_mov_b32_dpp v42, v16 quad_perm:[2,3,0,1] row_mask:0xf bank_mask:0xf bound_ctrl:1
	v_max_f32_e32 v42, v42, v42
	v_max_f32_e32 v16, v16, v42
	s_nop 1
	v_mov_b32_dpp v42, v16 row_half_mirror row_mask:0xf bank_mask:0xf bound_ctrl:1
	v_max_f32_e32 v42, v42, v42
	v_max_f32_e32 v16, v16, v42
	s_nop 1
	v_mov_b32_dpp v42, v16 row_mirror row_mask:0xf bank_mask:0xf bound_ctrl:1
	v_max_f32_e32 v42, v42, v42
	v_max_f32_e32 v16, v16, v42
	v_mov_b32_e32 v42, v16
	s_nop 1
	v_permlane16_swap_b32_e32 v16, v42
	v_max_f32_e32 v42, v42, v42
	v_max_f32_e32 v16, v16, v16
	v_max_f32_e32 v16, v16, v42
	v_mov_b32_e32 v42, v16
	s_nop 1
	v_permlane32_swap_b32_e32 v16, v42
	v_max_f32_e32 v42, v42, v42
	v_max_f32_e32 v16, v16, v16
	v_max_f32_e32 v16, v16, v42
	v_div_scale_f32 v42, s[14:15], v16, v16, s1
	v_rcp_f32_e32 v43, v42
	v_div_scale_f32 v44, vcc, s1, v16, s1
	v_fma_f32 v45, -v42, v43, 1.0
	v_fmac_f32_e32 v43, v45, v43
	v_mul_f32_e32 v45, v44, v43
	v_fma_f32 v46, -v42, v45, v44
	v_fmac_f32_e32 v45, v46, v43
	v_fma_f32 v42, -v42, v45, v44
	v_div_fmas_f32 v42, v42, v43, v45
	v_div_fixup_f32 v42, v42, v16, s1
	v_cmp_lt_f32_e32 vcc, 0, v16
	s_nop 1
	v_cndmask_b32_e32 v42, 0, v42, vcc
	v_mul_f32_e32 v21, v21, v42
	v_mul_f32_e32 v20, v20, v42
	v_mul_f32_e32 v22, v22, v42
	v_mul_f32_e32 v23, v23, v42
	v_mul_f32_e32 v25, v25, v42
	v_rndne_f32_e32 v21, v21
	v_mul_f32_e32 v24, v24, v42
	v_mul_f32_e32 v26, v26, v42
	v_mul_f32_e32 v27, v27, v42
	v_rndne_f32_e32 v20, v20
	v_rndne_f32_e32 v22, v22
	v_rndne_f32_e32 v23, v23
	v_rndne_f32_e32 v25, v25
	v_cvt_i32_f32_e32 v21, v21
	v_rndne_f32_e32 v24, v24
	v_rndne_f32_e32 v26, v26
	v_rndne_f32_e32 v27, v27
	v_cvt_i32_f32_e32 v20, v20
	v_cvt_i32_f32_sdwa v22, v22 dst_sel:WORD_1 dst_unused:UNUSED_PAD src0_sel:DWORD
	v_cvt_i32_f32_e32 v23, v23
	v_cvt_i32_f32_e32 v25, v25
	v_cvt_i32_f32_e32 v24, v24
	v_cvt_i32_f32_sdwa v26, v26 dst_sel:WORD_1 dst_unused:UNUSED_PAD src0_sel:DWORD
	v_cvt_i32_f32_e32 v27, v27
	v_lshlrev_b32_e32 v21, 8, v21
	v_and_b32_e32 v22, 0xff0000, v22
	v_perm_b32 v20, v23, v20, s5
	v_lshlrev_b32_e32 v23, 8, v25
	v_and_b32_e32 v21, 0xff00, v21
	v_mul_f32_e32 v29, v29, v42
	v_and_b32_e32 v25, 0xff0000, v26
	v_perm_b32 v24, v27, v24, s5
	v_and_b32_e32 v23, 0xff00, v23
	v_or3_b32 v20, v20, v21, v22
	v_mul_f32_e32 v28, v28, v42
	v_mul_f32_e32 v30, v30, v42
	v_mul_f32_e32 v31, v31, v42
	v_or3_b32 v21, v24, v23, v25
	global_store_dword v[40:41], v20, off
	global_store_dword v[40:41], v21, off offset:256
	v_rndne_f32_e32 v20, v29
	v_rndne_f32_e32 v28, v28
	v_cvt_i32_f32_e32 v20, v20
	v_rndne_f32_e32 v21, v30
	v_rndne_f32_e32 v22, v31
	v_cvt_i32_f32_e32 v28, v28
	v_cvt_i32_f32_sdwa v21, v21 dst_sel:WORD_1 dst_unused:UNUSED_PAD src0_sel:DWORD
	v_cvt_i32_f32_e32 v22, v22
	v_lshlrev_b32_e32 v20, 8, v20
	v_and_b32_e32 v20, 0xff00, v20
	v_and_b32_e32 v21, 0xff0000, v21
	v_perm_b32 v22, v22, v28, s5
	v_or3_b32 v20, v22, v20, v21
	v_mul_f32_e32 v21, v33, v42
	global_store_dword v[40:41], v20, off offset:512
	v_mul_f32_e32 v20, v32, v42
	v_mul_f32_e32 v22, v34, v42
	v_mul_f32_e32 v23, v35, v42
	v_rndne_f32_e32 v21, v21
	v_rndne_f32_e32 v20, v20
	v_cvt_i32_f32_e32 v21, v21
	v_rndne_f32_e32 v22, v22
	v_rndne_f32_e32 v23, v23
	v_cvt_i32_f32_e32 v20, v20
	v_cvt_i32_f32_sdwa v22, v22 dst_sel:WORD_1 dst_unused:UNUSED_PAD src0_sel:DWORD
	v_cvt_i32_f32_e32 v23, v23
	v_lshlrev_b32_e32 v21, 8, v21
	v_and_b32_e32 v21, 0xff00, v21
	v_and_b32_e32 v22, 0xff0000, v22
	v_perm_b32 v20, v23, v20, s5
	v_or3_b32 v20, v20, v21, v22
	v_mul_f32_e32 v21, v37, v42
	v_mul_f32_e32 v11, v11, v42
	v_mul_f32_e32 v7, v7, v42
	v_mul_f32_e32 v3, v3, v42
	global_store_dword v[40:41], v20, off offset:768
	v_mul_f32_e32 v20, v36, v42
	v_mul_f32_e32 v22, v38, v42
	v_mul_f32_e32 v23, v39, v42
	v_rndne_f32_e32 v21, v21
	v_mul_f32_e32 v10, v10, v42
	v_mul_f32_e32 v12, v12, v42
	v_mul_f32_e32 v13, v13, v42
	v_rndne_f32_e32 v11, v11
	v_mul_f32_e32 v6, v6, v42
	v_mul_f32_e32 v8, v8, v42
	v_mul_f32_e32 v9, v9, v42
	v_rndne_f32_e32 v7, v7
	v_mul_f32_e32 v2, v2, v42
	v_mul_f32_e32 v4, v4, v42
	v_mul_f32_e32 v5, v5, v42
	v_rndne_f32_e32 v3, v3
	v_rndne_f32_e32 v20, v20
	v_cvt_i32_f32_e32 v21, v21
	v_rndne_f32_e32 v22, v22
	v_rndne_f32_e32 v23, v23
	v_rndne_f32_e32 v10, v10
	v_cvt_i32_f32_e32 v11, v11
	v_rndne_f32_e32 v12, v12
	v_rndne_f32_e32 v13, v13
	v_rndne_f32_e32 v6, v6
	v_cvt_i32_f32_e32 v7, v7
	v_rndne_f32_e32 v8, v8
	v_rndne_f32_e32 v9, v9
	v_rndne_f32_e32 v2, v2
	v_cvt_i32_f32_e32 v3, v3
	v_rndne_f32_e32 v4, v4
	v_rndne_f32_e32 v5, v5
	v_cvt_i32_f32_e32 v20, v20
	v_cvt_i32_f32_sdwa v22, v22 dst_sel:WORD_1 dst_unused:UNUSED_PAD src0_sel:DWORD
	v_cvt_i32_f32_e32 v23, v23
	v_cvt_i32_f32_e32 v10, v10
	v_cvt_i32_f32_sdwa v12, v12 dst_sel:WORD_1 dst_unused:UNUSED_PAD src0_sel:DWORD
	v_cvt_i32_f32_e32 v13, v13
	v_cvt_i32_f32_e32 v6, v6
	v_cvt_i32_f32_sdwa v8, v8 dst_sel:WORD_1 dst_unused:UNUSED_PAD src0_sel:DWORD
	v_cvt_i32_f32_e32 v9, v9
	v_cvt_i32_f32_e32 v2, v2
	v_cvt_i32_f32_sdwa v4, v4 dst_sel:WORD_1 dst_unused:UNUSED_PAD src0_sel:DWORD
	v_cvt_i32_f32_e32 v5, v5
	v_lshlrev_b32_e32 v21, 8, v21
	v_lshlrev_b32_e32 v11, 8, v11
	v_lshlrev_b32_e32 v7, 8, v7
	v_lshlrev_b32_e32 v3, 8, v3
	v_and_b32_e32 v21, 0xff00, v21
	v_and_b32_e32 v22, 0xff0000, v22
	v_perm_b32 v20, v23, v20, s5
	v_and_b32_e32 v11, 0xff00, v11
	v_and_b32_e32 v12, 0xff0000, v12
	v_perm_b32 v10, v13, v10, s5
	v_and_b32_e32 v7, 0xff00, v7
	v_and_b32_e32 v8, 0xff0000, v8
	v_perm_b32 v6, v9, v6, s5
	v_and_b32_e32 v3, 0xff00, v3
	v_and_b32_e32 v4, 0xff0000, v4
	v_perm_b32 v2, v5, v2, s5
	v_or3_b32 v20, v20, v21, v22
	v_or3_b32 v10, v10, v11, v12
	v_or3_b32 v6, v6, v7, v8
	v_or3_b32 v2, v2, v3, v4
	global_store_dword v[40:41], v20, off offset:1024
	global_store_dword v[40:41], v10, off offset:1280
	global_store_dword v[40:41], v6, off offset:1536
	global_store_dword v[40:41], v2, off offset:1792
	s_and_saveexec_b64 s[14:15], s[6:7]
	s_cbranch_execz .LBB0_67
	s_add_u32 s18, s92, s3
	s_addc_u32 s19, s93, s16
	v_mul_f32_e32 v2, 0x3c010204, v16
	global_store_dword v17, v2, s[18:19]
	s_branch .LBB0_67
